# v27 = v25 + GLA-scan conversion stores at default cache policy
# speedup vs baseline: 1.0040x; 1.0040x over previous
; #define CT_LOADNT(T_) do { const int tt_ = (T_) < CT_TOTAL ? (T_) : CT_TOTAL - 1; const ConvTile ct_ = conv_tile_desc(cttab, tt_); const int ckq_ = lane >> 4, ccol_ = ((lane & 15) * 4 < ct_.nvalid) ? (lane & 15) * 4 : 0; CT_FORQ(CT_LOAD1NT) } while (0)
; #define CT_STORENT(T_) do { const int tt_ = (T_) < CT_TOTAL ? (T_) : CT_TOTAL - 1; const ConvTile ct_ = conv_tile_desc(cttab, tt_); const bool cok_ = (lane & 15) * 4 < ct_.nvalid; \
;     bf16_t* cdst_ = ct_.dst + (size_t)((lane & 15) * 4) * ct_.K + (lane >> 4) * 8; CT_ATOMNT(0, x) CT_ATOMNT(1, y) CT_ATOMNT(2, z) CT_ATOMNT(3, w) } while (0)
; __device__ __forceinline__ void ph_glascan(const Params& p, float* lds, int wg, int nwg, int gct_begin) {
;     ...
;             {
;                 const int tconv = gct_begin + c * (nwg * 8) + wg * 8 + w;
;                 if (c < gct_nch) { CT_STORENT(tconv); if (c + 1 < gct_nch) CT_LOADNT(tconv + nwg * 8); }
;             }
.LBB0_1597:
	s_lshl_b32 s46, s46, 6
	s_sub_i32 s52, s25, s46
	s_and_b64 s[56:57], s[56:57], exec
	s_cselect_b32 s52, 64, s52
	s_lshl_b32 s44, s44, 3
	s_add_i32 s44, s44, 0
	s_add_i32 s44, s44, 0x20040
	v_mov_b32_e32 v2, s44
	ds_read_b64 v[6:7], v2
	s_mul_i32 s25, s6, s25
	v_lshlrev_b32_e64 v2, v4, s25
	v_mul_hi_u32 v5, v2, s54
	v_mul_lo_u32 v4, v2, s54
	s_lshl_b32 s56, s7, 5
	v_lshlrev_b64 v[4:5], 1, v[4:5]
	s_mul_hi_i32 s55, s6, s46
	s_mul_i32 s54, s6, s46
	s_ashr_i32 s57, s56, 31
	s_waitcnt lgkmcnt(0)
	v_lshl_add_u64 v[4:5], v[6:7], 0, v[4:5]
	s_lshl_b64 s[54:55], s[54:55], 1
	v_lshl_add_u64 v[4:5], v[4:5], 0, s[54:55]
	s_lshl_b64 s[54:55], s[56:57], 1
	v_mul_u32_u24_e32 v2, s6, v164
	v_lshl_add_u64 v[4:5], v[4:5], 0, s[54:55]
	v_lshlrev_b32_e32 v2, 1, v2
	v_lshl_add_u64 v[4:5], v[4:5], 0, v[2:3]
	v_lshlrev_b32_e32 v2, 1, v162
	v_lshl_add_u64 v[8:9], v[4:5], 0, v[2:3]
	v_cvt_pk_bf16_f32 v2, v74, v78
	v_cvt_pk_bf16_f32 v4, v86, v94
	v_cvt_pk_bf16_f32 v5, v102, v114
	v_cvt_pk_bf16_f32 v6, v126, v130
	v_cmp_gt_i32_e32 vcc, s52, v164
	s_lshl_b32 s52, s6, 1
	s_nop 0
	v_cndmask_b32_e32 v7, 0, v6, vcc
	v_cndmask_b32_e32 v6, 0, v5, vcc
	v_cndmask_b32_e32 v5, 0, v4, vcc
	v_cndmask_b32_e32 v4, 0, v2, vcc
	global_store_dwordx4 v[8:9], v[4:7], off
	v_cvt_pk_bf16_f32 v2, v75, v79
	v_lshl_add_u64 v[8:9], v[8:9], 0, s[52:53]
	v_cvt_pk_bf16_f32 v4, v87, v95
	v_cvt_pk_bf16_f32 v5, v103, v115
	v_cvt_pk_bf16_f32 v6, v127, v131
	v_cndmask_b32_e32 v7, 0, v6, vcc
	v_cndmask_b32_e32 v6, 0, v5, vcc
	v_cndmask_b32_e32 v5, 0, v4, vcc
	v_cndmask_b32_e32 v4, 0, v2, vcc
	global_store_dwordx4 v[8:9], v[4:7], off
	v_cvt_pk_bf16_f32 v2, v76, v80
	v_lshl_add_u64 v[8:9], v[8:9], 0, s[52:53]
	v_cvt_pk_bf16_f32 v4, v88, v96
	v_cvt_pk_bf16_f32 v5, v104, v116
	v_cvt_pk_bf16_f32 v6, v128, v132
	v_cndmask_b32_e32 v7, 0, v6, vcc
	v_cndmask_b32_e32 v6, 0, v5, vcc
	v_cndmask_b32_e32 v5, 0, v4, vcc
	v_cndmask_b32_e32 v4, 0, v2, vcc
	global_store_dwordx4 v[8:9], v[4:7], off
	v_cvt_pk_bf16_f32 v2, v77, v81
	v_lshl_add_u64 v[8:9], v[8:9], 0, s[52:53]
	v_cvt_pk_bf16_f32 v4, v89, v97
	v_cvt_pk_bf16_f32 v5, v105, v117
	v_cvt_pk_bf16_f32 v6, v129, v133
	v_cndmask_b32_e32 v7, 0, v6, vcc
	v_cndmask_b32_e32 v6, 0, v5, vcc
	v_cndmask_b32_e32 v5, 0, v4, vcc
	v_cndmask_b32_e32 v4, 0, v2, vcc
	global_store_dwordx4 v[8:9], v[4:7], off

; #define CT_LOADNT(T_) do { const int tt_ = (T_) < CT_TOTAL ? (T_) : CT_TOTAL - 1; const ConvTile ct_ = conv_tile_desc(cttab, tt_); const int ckq_ = lane >> 4, ccol_ = ((lane & 15) * 4 < ct_.nvalid) ? (lane & 15) * 4 : 0; CT_FORQ(CT_LOAD1NT) } while (0)
; #define CT_STORENT(T_) do { const int tt_ = (T_) < CT_TOTAL ? (T_) : CT_TOTAL - 1; const ConvTile ct_ = conv_tile_desc(cttab, tt_); const bool cok_ = (lane & 15) * 4 < ct_.nvalid; \
;     bf16_t* cdst_ = ct_.dst + (size_t)((lane & 15) * 4) * ct_.K + (lane >> 4) * 8; CT_ATOMNT(0, x) CT_ATOMNT(1, y) CT_ATOMNT(2, z) CT_ATOMNT(3, w) } while (0)
; __device__ __forceinline__ void ph_glascan(const Params& p, float* lds, int wg, int nwg, int gct_begin) {
;     ...
;             {
;                 const int tconv = gct_begin + c * (nwg * 8) + wg * 8 + w;
;                 if (c < gct_nch) { CT_STORENT(tconv); if (c + 1 < gct_nch) CT_LOADNT(tconv + nwg * 8); }
;             }
.Lgla_wd:
	v_cvt_pk_bf16_f32 v2, v74, v78
	v_cvt_pk_bf16_f32 v134, v86, v94
	v_cvt_pk_bf16_f32 v135, v102, v114
	v_cvt_pk_bf16_f32 v136, v126, v130
	v_cmp_gt_i32_e32 vcc, s63, v164
	s_lshl_b64 s[56:57], s[56:57], 1
	s_cmp_ge_i32 s44, s69
	v_cndmask_b32_e32 v137, 0, v136, vcc
	v_cndmask_b32_e32 v136, 0, v135, vcc
	v_cndmask_b32_e32 v135, 0, v134, vcc
	v_cndmask_b32_e32 v134, 0, v2, vcc
	global_store_dwordx4 v[4:5], v[134:137], off
	v_cvt_pk_bf16_f32 v2, v75, v79
	v_lshl_add_u64 v[4:5], v[4:5], 0, s[56:57]
	v_cvt_pk_bf16_f32 v134, v87, v95
	v_cvt_pk_bf16_f32 v135, v103, v115
	v_cvt_pk_bf16_f32 v136, v127, v131
	v_cndmask_b32_e32 v137, 0, v136, vcc
	v_cndmask_b32_e32 v136, 0, v135, vcc
	v_cndmask_b32_e32 v135, 0, v134, vcc
	v_cndmask_b32_e32 v134, 0, v2, vcc
	global_store_dwordx4 v[4:5], v[134:137], off
	v_cvt_pk_bf16_f32 v2, v76, v80
	v_lshl_add_u64 v[4:5], v[4:5], 0, s[56:57]
	v_cvt_pk_bf16_f32 v134, v88, v96
	v_cvt_pk_bf16_f32 v135, v104, v116
	v_cvt_pk_bf16_f32 v136, v128, v132
	v_cndmask_b32_e32 v137, 0, v136, vcc
	v_cndmask_b32_e32 v136, 0, v135, vcc
	v_cndmask_b32_e32 v135, 0, v134, vcc
	v_cndmask_b32_e32 v134, 0, v2, vcc
	global_store_dwordx4 v[4:5], v[134:137], off
	v_cvt_pk_bf16_f32 v2, v77, v81
	v_lshl_add_u64 v[4:5], v[4:5], 0, s[56:57]
	v_cvt_pk_bf16_f32 v134, v89, v97
	v_cvt_pk_bf16_f32 v135, v105, v117
	v_cvt_pk_bf16_f32 v136, v129, v133
	v_cndmask_b32_e32 v137, 0, v136, vcc
	v_cndmask_b32_e32 v136, 0, v135, vcc
	v_cndmask_b32_e32 v135, 0, v134, vcc
	v_cndmask_b32_e32 v134, 0, v2, vcc
	global_store_dwordx4 v[4:5], v[134:137], off
	s_cbranch_scc1 .LBB0_1681
	s_mul_i32 vcc_lo, s84, 0x228
	s_add_i32 vcc_lo, vcc_lo, s93
	s_min_i32 s90, vcc_lo, 0x324ff
	s_cmpk_gt_i32 vcc_lo, 0x19ff
	s_mov_b64 s[62:63], -1
	s_cbranch_scc0 .LBB0_1678
	s_cmpk_gt_u32 vcc_lo, 0x21ff
	s_cbranch_scc0 .LBB0_1675
	s_cmpk_gt_u32 vcc_lo, 0x4dff
	s_cbranch_scc0 .LBB0_1672
	s_cmpk_gt_u32 vcc_lo, 0x63ff
	s_cbranch_scc0 .LBB0_1669
	s_mov_b64 s[56:57], -1
	s_cmpk_gt_u32 vcc_lo, 0x7cff
	s_cbranch_scc0 .LBB0_1666
	s_cmpk_gt_u32 vcc_lo, 0x84ff
	s_cbranch_scc0 .LBB0_1663
	s_mov_b64 s[58:59], -1
	s_cmp_gt_u32 vcc_lo, 0x244ff
	s_mov_b64 s[60:61], -1
	s_cbranch_scc0 .LBB0_1661
	s_add_i32 s25, s90, 0xbb00
	s_bfe_u32 s46, s25, 0x6000a
	s_mulk_i32 s46, 0x2493
	s_lshr_b32 s46, s46, 16
	s_mul_i32 s52, s46, 0x1c00
	s_sub_i32 s25, s25, s52
	s_and_b32 s92, s25, 31
	s_bfe_u32 s91, s25, 0xb0005
	s_mov_b64 s[60:61], 0
